# MLA attention: waves 4-7 defer softmax+PV of each tile by one step (run beside the other half's QK), V tiles triple-buffered in 16 KiB extra static LDS, one drain step per unit
# baseline (speedup 1.0000x reference)
; #define LAS __attribute__((address_space(3)))
; __device__ __forceinline__ float bf2f(bf16 b) { return __uint_as_float(((unsigned)b) << 16); }
; __device__ __forceinline__ void mla_attn_phase(LAS unsigned char* lds, const bf16* Q, const bf16* KV, const bf16* Z, bf16* Oabc, const float* ropec, const float* ropes, int vcu, int G, int tid) {
;     ...
;             const int qb = half ? 15 - (pi & 7) : (pi & 7);
;             bf16x8 qr[8];
;             { bf16x8 qrope[4]; unsigned qoff_ = qoff, roff_ = roff; asm volatile("" : "+v"(qoff_), "+v"(roff_));
;               const char* Qu = (const char*)(Q + (tok0 + qb * 256) * 1536 + h * 192);
;               const char* cu = (const char*)(ropec + (size_t)(qb * 256) * 32); const char* su = (const char*)(ropes + (size_t)(qb * 256) * 32);
; #pragma unroll
;               for (int d0 = 0; d0 < 8; ++d0) qr[d0] = *(const bf16x8*)(Qu + qoff_ + d0 * 32);
; #pragma unroll
;               for (int d0 = 0; d0 < 4; ++d0) qrope[d0] = *(const bf16x8*)(Qu + qoff_ + (8 + d0) * 32);
; #pragma unroll
;               for (int pr = 0; pr < 2; ++pr) {
;                   const f32x4 c0 = *(const f32x4*)(cu + roff_ + pr * 64), c1 = *(const f32x4*)(cu + roff_ + pr * 64 + 16), s0 = *(const f32x4*)(su + roff_ + pr * 64), s1 = *(const f32x4*)(su + roff_ + pr * 64 + 16);
;                   const float cc[8] = {c0.x, c0.y, c0.z, c0.w, c1.x, c1.y, c1.z, c1.w}, ss[8] = {s0.x, s0.y, s0.z, s0.w, s1.x, s1.y, s1.z, s1.w};
;                   bf16x8 xa = qrope[pr], xb = qrope[2 + pr];
; #pragma unroll
;                   for (int e = 0; e < 8; ++e) { const float x1 = bf2f((bf16)xa[e]), x2 = bf2f((bf16)xb[e]);
;                       xa[e] = (short)f2bf(x1 * cc[e] - x2 * ss[e]); xb[e] = (short)f2bf(x1 * ss[e] + x2 * cc[e]); }
;                   *(LAS bf16x8*)(qrl + (pr * 64 + lane) * 16) = xa; *(LAS bf16x8*)(qrl + ((2 + pr) * 64 + lane) * 16) = xb; } }
;             v4u vs0, vs1, ks0, ks1, krr;
;             const char* KVu = (const char*)(KV + tok0 * 2048 + h * 256); const char* Zu = (const char*)(Z + tok0 * NABC);
;     ...
;             const int nt = 4 * qb + 4;
;             float m_reg = -1e30f, l_reg = 0.f; f32x16 o[4];
; #pragma unroll
;             for (int d = 0; d < 4; ++d)
; #pragma unroll
;                 for (int r = 0; r < 16; ++r) o[d][r] = 0.f;
;             MLA_SLOAD(0); MLA_SWRITE(0); __syncthreads();
.LBB0_1124:
	s_xor_b64 s[12:13], s[6:7], -1
	s_and_b64 s[6:7], s[6:7], exec
	s_cselect_b32 s17, s29, s30
	s_lshl_b32 s16, s17, 8
	s_or_b32 s38, s10, s16
	s_mul_hi_u32 s7, s38, 0xc00
	s_mul_i32 s14, s11, 0xc00
	s_mul_i32 s6, s38, 0xc00
	s_add_i32 s7, s7, s14
	s_add_u32 s14, s31, s6
	s_addc_u32 s15, s34, s7
	s_lshl_b32 s44, s17, 15
	v_mov_b32_e32 v6, v207
	v_mov_b32_e32 v0, v208
	s_add_u32 s6, s20, s44
	s_addc_u32 s7, s21, 0
	global_load_dwordx4 v[112:115], v6, s[14:15]
	global_load_dwordx4 v[116:119], v6, s[14:15] offset:32
	global_load_dwordx4 v[120:123], v6, s[14:15] offset:64
	global_load_dwordx4 v[124:127], v6, s[14:15] offset:96
	global_load_dwordx4 v[128:131], v6, s[14:15] offset:128
	global_load_dwordx4 v[132:135], v6, s[14:15] offset:160
	global_load_dwordx4 v[136:139], v6, s[14:15] offset:192
	global_load_dwordx4 v[140:143], v6, s[14:15] offset:224
	global_load_dwordx4 v[10:13], v6, s[14:15] offset:256
	global_load_dwordx4 v[2:5], v6, s[14:15] offset:288
	global_load_dwordx4 v[14:17], v6, s[14:15] offset:320
	s_nop 0
	global_load_dwordx4 v[6:9], v6, s[14:15] offset:352
	s_add_u32 s14, s22, s44
	s_addc_u32 s15, s23, 0
	global_load_dwordx4 v[18:21], v0, s[6:7] offset:16
	global_load_dwordx4 v[22:25], v0, s[6:7]
	global_load_dwordx4 v[26:29], v0, s[14:15] offset:16
	global_load_dwordx4 v[30:33], v0, s[14:15]
	v_add_u32_e32 v214, s25, v209
	s_mov_b32 s39, s11
	v_add_u32_e32 v215, s16, v205
	v_mov_b32_e32 v217, 0
	v_mov_b32_e32 v216, 0xf149f2ca
	s_mov_b32 s50, 1
	v_readlane_b32 s32, v252, 37
	s_mov_b32 s69, 0x18000
	s_mov_b32 s94, 0
	s_mov_b32 s98, 0x4000
	s_nop 1
	s_lshr_b32 s32, s32, 8
	v_lshl_add_u32 v215, s32, 6, v215
	v_mov_b64_e32 v[194:195], v[192:193]
	v_mov_b64_e32 v[196:197], v[190:191]
	s_waitcnt vmcnt(0)
	v_and_b32_e32 v35, 0xffff0000, v10
	v_lshlrev_b32_e32 v34, 16, v10
	v_and_b32_e32 v37, 0xffff0000, v14
	v_lshlrev_b32_e32 v36, 16, v14
	v_lshlrev_b32_e32 v10, 16, v15
	v_pk_mul_f32 v[38:39], v[30:31], v[34:35]
	v_pk_mul_f32 v[30:31], v[30:31], v[36:37]
	v_pk_fma_f32 v[38:39], v[22:23], v[36:37], v[38:39]
	v_pk_fma_f32 v[22:23], v[22:23], v[34:35], v[30:31] neg_lo:[0,0,1] neg_hi:[0,0,1]
	v_and_b32_e32 v31, 0xffff0000, v11
	v_lshlrev_b32_e32 v30, 16, v11
	v_and_b32_e32 v11, 0xffff0000, v15
	v_pk_mul_f32 v[14:15], v[32:33], v[30:31]
	s_nop 0
	v_pk_fma_f32 v[14:15], v[24:25], v[10:11], v[14:15]
	v_pk_mul_f32 v[10:11], v[32:33], v[10:11]
	s_nop 0
	v_pk_fma_f32 v[10:11], v[24:25], v[30:31], v[10:11] neg_lo:[0,0,1] neg_hi:[0,0,1]
	v_and_b32_e32 v25, 0xffff0000, v12
	v_lshlrev_b32_e32 v24, 16, v12
	v_and_b32_e32 v31, 0xffff0000, v16
	v_lshlrev_b32_e32 v30, 16, v16
	v_pk_mul_f32 v[32:33], v[26:27], v[24:25]
	v_pk_mul_f32 v[26:27], v[26:27], v[30:31]
	v_pk_fma_f32 v[32:33], v[18:19], v[30:31], v[32:33]
	v_pk_fma_f32 v[18:19], v[18:19], v[24:25], v[26:27] neg_lo:[0,0,1] neg_hi:[0,0,1]
	v_and_b32_e32 v25, 0xffff0000, v13
	v_lshlrev_b32_e32 v24, 16, v13
	v_and_b32_e32 v13, 0xffff0000, v17
	v_lshlrev_b32_e32 v12, 16, v17
	v_pk_mul_f32 v[16:17], v[28:29], v[24:25]
	v_bfe_u32 v26, v11, 16, 1
	v_pk_fma_f32 v[16:17], v[20:21], v[12:13], v[16:17]
	v_pk_mul_f32 v[12:13], v[28:29], v[12:13]
	v_bfe_u32 v27, v10, 16, 1
	v_pk_fma_f32 v[12:13], v[20:21], v[24:25], v[12:13] neg_lo:[0,0,1] neg_hi:[0,0,1]
	v_bfe_u32 v24, v19, 16, 1
	v_bfe_u32 v20, v13, 16, 1
	v_bfe_u32 v21, v12, 16, 1
	v_bfe_u32 v25, v18, 16, 1
	v_bfe_u32 v28, v23, 16, 1
	v_bfe_u32 v29, v22, 16, 1
	v_add3_u32 v22, v22, v29, s40
	v_add3_u32 v23, v23, v28, s40
	v_add3_u32 v10, v10, v27, s40
	v_add3_u32 v11, v11, v26, s40
	v_add3_u32 v18, v18, v25, s40
	v_add3_u32 v19, v19, v24, s40
	v_add3_u32 v12, v12, v21, s40
	v_add3_u32 v13, v13, v20, s40
	v_perm_b32 v13, v13, v12, s48
	v_perm_b32 v12, v19, v18, s48
	v_perm_b32 v11, v11, v10, s48
	v_perm_b32 v10, v23, v22, s48
	v_bfe_u32 v18, v17, 16, 1
	v_bfe_u32 v19, v16, 16, 1
	v_bfe_u32 v20, v33, 16, 1
	v_bfe_u32 v21, v32, 16, 1
	v_bfe_u32 v22, v15, 16, 1
	v_bfe_u32 v23, v14, 16, 1
	v_bfe_u32 v24, v39, 16, 1
	v_bfe_u32 v25, v38, 16, 1
	v_add3_u32 v25, v38, v25, s40
	v_add3_u32 v24, v39, v24, s40
	v_add3_u32 v14, v14, v23, s40
	v_add3_u32 v15, v15, v22, s40
	v_add3_u32 v21, v32, v21, s40
	v_add3_u32 v20, v33, v20, s40
	v_add3_u32 v16, v16, v19, s40
	v_add3_u32 v17, v17, v18, s40
	v_perm_b32 v17, v17, v16, s48
	v_perm_b32 v16, v20, v21, s48
	v_perm_b32 v15, v15, v14, s48
	v_perm_b32 v14, v24, v25, s48
	ds_write_b128 v214, v[10:13]
	ds_write_b128 v214, v[14:17] offset:2048
	global_load_dwordx4 v[10:13], v0, s[6:7] offset:80
	global_load_dwordx4 v[14:17], v0, s[6:7] offset:64
	global_load_dwordx4 v[18:21], v0, s[14:15] offset:80
	global_load_dwordx4 v[22:25], v0, s[14:15] offset:64
	v_and_b32_e32 v27, 0xffff0000, v2
	v_lshlrev_b32_e32 v26, 16, v2
	v_and_b32_e32 v29, 0xffff0000, v6
	v_lshlrev_b32_e32 v28, 16, v6
	v_lshlrev_b32_e32 v2, 16, v7
	s_lshl_b32 s6, s17, 2
	s_add_i32 s44, s6, 4
	s_sub_i32 s45, 0, s6
	s_waitcnt vmcnt(0)
; #define LAS __attribute__((address_space(3)))
; __device__ __forceinline__ unsigned f2bf(float f) { unsigned u = __builtin_bit_cast(unsigned, f); return (u + 0x7fffu + ((u >> 16) & 1u)) >> 16; }
; __device__ __forceinline__ float bf2f(bf16 b) { return __uint_as_float(((unsigned)b) << 16); }
; #define MLA_SLOAD(k0) do { const char* kvp = KVu + (size_t)(k0) * 4096; const char* zp = Zu + (size_t)(k0) * (NABC * 2); \
;             ks0 = *(const v4u*)(kvp + kvoff); vs0 = *(const v4u*)(kvp + kvoff + 256); ks1 = *(const v4u*)(kvp + 32 * 4096 + kvoff); vs1 = *(const v4u*)(kvp + 32 * 4096 + kvoff + 256); \
;             krr = *(const v4u*)(zp + zoff); } while (0)
; __device__ __forceinline__ void mla_attn_phase(LAS unsigned char* lds, const bf16* Q, const bf16* KV, const bf16* Z, bf16* Oabc, const float* ropec, const float* ropes, int vcu, int G, int tid) {
;     ...
;               for (int pr = 0; pr < 2; ++pr) {
;                   const f32x4 c0 = *(const f32x4*)(cu + roff_ + pr * 64), c1 = *(const f32x4*)(cu + roff_ + pr * 64 + 16), s0 = *(const f32x4*)(su + roff_ + pr * 64), s1 = *(const f32x4*)(su + roff_ + pr * 64 + 16);
;                   const float cc[8] = {c0.x, c0.y, c0.z, c0.w, c1.x, c1.y, c1.z, c1.w}, ss[8] = {s0.x, s0.y, s0.z, s0.w, s1.x, s1.y, s1.z, s1.w};
;                   bf16x8 xa = qrope[pr], xb = qrope[2 + pr];
; #pragma unroll
;                   for (int e = 0; e < 8; ++e) { const float x1 = bf2f((bf16)xa[e]), x2 = bf2f((bf16)xb[e]);
;                       xa[e] = (short)f2bf(x1 * cc[e] - x2 * ss[e]); xb[e] = (short)f2bf(x1 * ss[e] + x2 * cc[e]); }
;                   *(LAS bf16x8*)(qrl + (pr * 64 + lane) * 16) = xa; *(LAS bf16x8*)(qrl + ((2 + pr) * 64 + lane) * 16) = xb; } }
;             v4u vs0, vs1, ks0, ks1, krr;
;             const char* KVu = (const char*)(KV + tok0 * 2048 + h * 256); const char* Zu = (const char*)(Z + tok0 * NABC);
;     ...
;             const int nt = 4 * qb + 4;
;             float m_reg = -1e30f, l_reg = 0.f; f32x16 o[4];
; #pragma unroll
;             for (int d = 0; d < 4; ++d)
; #pragma unroll
;                 for (int r = 0; r < 16; ++r) o[d][r] = 0.f;
;             MLA_SLOAD(0); MLA_SWRITE(0); __syncthreads();
; #pragma unroll 1
;             for (int t = 0; t < nt; ++t) {
;                 const int buf = t & 1;
;                 if (t + 1 < nt) MLA_SLOAD((t + 1) * 64);
	v_pk_mul_f32 v[30:31], v[22:23], v[26:27]
	v_pk_mul_f32 v[22:23], v[22:23], v[28:29]
	v_pk_fma_f32 v[30:31], v[14:15], v[28:29], v[30:31]
	v_pk_fma_f32 v[14:15], v[14:15], v[26:27], v[22:23] neg_lo:[0,0,1] neg_hi:[0,0,1]
	v_and_b32_e32 v23, 0xffff0000, v3
	v_lshlrev_b32_e32 v22, 16, v3
	v_and_b32_e32 v3, 0xffff0000, v7
	v_pk_mul_f32 v[6:7], v[24:25], v[22:23]
	s_nop 0
	v_pk_fma_f32 v[6:7], v[16:17], v[2:3], v[6:7]
	v_pk_mul_f32 v[2:3], v[24:25], v[2:3]
	s_nop 0
	v_pk_fma_f32 v[2:3], v[16:17], v[22:23], v[2:3] neg_lo:[0,0,1] neg_hi:[0,0,1]
	v_and_b32_e32 v17, 0xffff0000, v4
	v_lshlrev_b32_e32 v16, 16, v4
	v_and_b32_e32 v23, 0xffff0000, v8
	v_lshlrev_b32_e32 v22, 16, v8
	v_pk_mul_f32 v[24:25], v[18:19], v[16:17]
	v_pk_mul_f32 v[18:19], v[18:19], v[22:23]
	v_pk_fma_f32 v[24:25], v[10:11], v[22:23], v[24:25]
	v_pk_fma_f32 v[10:11], v[10:11], v[16:17], v[18:19] neg_lo:[0,0,1] neg_hi:[0,0,1]
	v_and_b32_e32 v17, 0xffff0000, v5
	v_lshlrev_b32_e32 v16, 16, v5
	v_and_b32_e32 v5, 0xffff0000, v9
	v_lshlrev_b32_e32 v4, 16, v9
	v_pk_mul_f32 v[8:9], v[20:21], v[16:17]
	v_bfe_u32 v0, v11, 16, 1
	v_pk_fma_f32 v[8:9], v[12:13], v[4:5], v[8:9]
	v_pk_mul_f32 v[4:5], v[20:21], v[4:5]
	v_bfe_u32 v20, v2, 16, 1
	v_pk_fma_f32 v[4:5], v[12:13], v[16:17], v[4:5] neg_lo:[0,0,1] neg_hi:[0,0,1]
	v_bfe_u32 v12, v10, 16, 1
	v_bfe_u32 v13, v15, 16, 1
	v_bfe_u32 v16, v14, 16, 1
	v_bfe_u32 v18, v4, 16, 1
	v_bfe_u32 v17, v5, 16, 1
	v_bfe_u32 v19, v3, 16, 1
	v_add3_u32 v20, v2, v20, s40
	v_add3_u32 v18, v4, v18, s40
	v_add3_u32 v2, v14, v16, s40
	v_add3_u32 v13, v15, v13, s40
	v_add3_u32 v4, v10, v12, s40
	v_add3_u32 v0, v11, v0, s40
	v_add3_u32 v3, v3, v19, s40
	v_add3_u32 v5, v5, v17, s40
	v_perm_b32 v4, v0, v4, s48
	v_perm_b32 v2, v13, v2, s48
	v_bfe_u32 v0, v25, 16, 1
	v_bfe_u32 v10, v24, 16, 1
	v_bfe_u32 v11, v31, 16, 1
	v_bfe_u32 v12, v30, 16, 1
	v_bfe_u32 v13, v9, 16, 1
	v_bfe_u32 v14, v8, 16, 1
	v_bfe_u32 v15, v7, 16, 1
	v_bfe_u32 v16, v6, 16, 1
	v_perm_b32 v5, v5, v18, s48
	v_perm_b32 v3, v3, v20, s48
	v_add3_u32 v16, v6, v16, s40
	v_add3_u32 v7, v7, v15, s40
	v_add3_u32 v14, v8, v14, s40
	v_add3_u32 v9, v9, v13, s40
	v_add3_u32 v6, v30, v12, s40
	v_add3_u32 v11, v31, v11, s40
	v_add3_u32 v8, v24, v10, s40
	v_add3_u32 v0, v25, v0, s40
	v_perm_b32 v8, v0, v8, s48
	v_perm_b32 v6, v11, v6, s48
	v_perm_b32 v9, v9, v14, s48
	v_perm_b32 v7, v7, v16, s48
	ds_write_b128 v214, v[2:5] offset:1024
	ds_write_b128 v214, v[6:9] offset:3072
	global_load_dwordx4 v[144:147], v[172:173], off
	global_load_dwordx4 v[148:151], v[172:173], off offset:256
	global_load_dwordx4 v[152:155], v[174:175], off
	global_load_dwordx4 v[156:159], v[174:175], off offset:256
	global_load_dwordx4 v[160:163], v[176:177], off
	v_add_u32_e32 v0, 0, v204
	s_waitcnt vmcnt(3)
	ds_write_b128 v210, v[148:151] offset:49152
	s_waitcnt vmcnt(1)
	ds_write_b128 v210, v[156:159] offset:57344
	ds_write_b128 v0, v[144:147]
	ds_write_b128 v0, v[152:155] offset:12288
	v_add_u32_e32 v0, 0, v199
	v_mov_b32_e32 v14, v1
	v_mov_b32_e32 v15, v1
	s_waitcnt vmcnt(0)
	ds_write_b128 v0, v[160:163]
	v_mov_b32_e32 v0, v1
	v_mov_b32_e32 v2, v1
	v_mov_b32_e32 v3, v1
	v_mov_b32_e32 v4, v1
	v_mov_b32_e32 v5, v1
	v_mov_b32_e32 v6, v1
	v_mov_b32_e32 v7, v1
	v_mov_b32_e32 v8, v1
	v_mov_b32_e32 v9, v1
	v_mov_b32_e32 v10, v1
	v_mov_b32_e32 v11, v1
	v_mov_b32_e32 v12, v1
	v_mov_b32_e32 v13, v1
	v_mov_b64_e32 v[30:31], v[14:15]
	v_mov_b64_e32 v[46:47], v[14:15]
	v_mov_b64_e32 v[62:63], v[14:15]
	v_mov_b64_e32 v[78:79], v[14:15]
	v_mov_b64_e32 v[28:29], v[12:13]
	v_mov_b64_e32 v[26:27], v[10:11]
	v_mov_b64_e32 v[24:25], v[8:9]
	v_mov_b64_e32 v[22:23], v[6:7]
	v_mov_b64_e32 v[20:21], v[4:5]
	v_mov_b64_e32 v[18:19], v[2:3]
	v_mov_b64_e32 v[16:17], v[0:1]
	v_mov_b64_e32 v[44:45], v[12:13]
	v_mov_b64_e32 v[42:43], v[10:11]
	v_mov_b64_e32 v[40:41], v[8:9]
	v_mov_b64_e32 v[38:39], v[6:7]
	v_mov_b64_e32 v[36:37], v[4:5]
	v_mov_b64_e32 v[34:35], v[2:3]
	v_mov_b64_e32 v[32:33], v[0:1]
	v_mov_b64_e32 v[60:61], v[12:13]
	v_mov_b64_e32 v[58:59], v[10:11]
	v_mov_b64_e32 v[56:57], v[8:9]
	v_mov_b64_e32 v[54:55], v[6:7]
	v_mov_b64_e32 v[52:53], v[4:5]
	v_mov_b64_e32 v[50:51], v[2:3]
	v_mov_b64_e32 v[48:49], v[0:1]
	v_mov_b64_e32 v[76:77], v[12:13]
	v_mov_b64_e32 v[74:75], v[10:11]
	v_mov_b64_e32 v[72:73], v[8:9]
	v_mov_b64_e32 v[70:71], v[6:7]
	v_mov_b64_e32 v[68:69], v[4:5]
	v_mov_b64_e32 v[66:67], v[2:3]
	v_mov_b64_e32 v[64:65], v[0:1]
	s_waitcnt lgkmcnt(0)
	s_barrier
	s_cmp_lt_u32 s50, s44
	s_cselect_b64 s[14:15], -1, 0
	s_cmp_ge_u32 s50, s44
	s_cbranch_scc1 .LBB0_1127
	s_branch .LBB0_1126
.LBB0_1125:
	s_cmp_lt_u32 s50, s44
	s_cselect_b64 s[14:15], -1, 0
	s_cmp_ge_u32 s50, s44
	s_cbranch_scc1 .LBB0_1127

; #define LAS __attribute__((address_space(3)))
; #define FA_SBAR() __builtin_amdgcn_sched_barrier(0)
; #define MLA_SLOAD(k0) do { const char* kvp = KVu + (size_t)(k0) * 4096; const char* zp = Zu + (size_t)(k0) * (NABC * 2); \
;             ks0 = *(const v4u*)(kvp + kvoff); vs0 = *(const v4u*)(kvp + kvoff + 256); ks1 = *(const v4u*)(kvp + 32 * 4096 + kvoff); vs1 = *(const v4u*)(kvp + 32 * 4096 + kvoff + 256); \
;             krr = *(const v4u*)(zp + zoff); } while (0)
; __device__ __forceinline__ void mla_attn_phase(LAS unsigned char* lds, const bf16* Q, const bf16* KV, const bf16* Z, bf16* Oabc, const float* ropec, const float* ropes, int vcu, int G, int tid) {
;     ...
;             for (int t = 0; t < nt; ++t) {
;                 const int buf = t & 1;
;                 if (t + 1 < nt) MLA_SLOAD((t + 1) * 64);
;                 FA_SBAR();
;                 const int tt = t - 4 * qb;
;                 {
;                     f32x16 p0, p1;
; #pragma unroll
;                     for (int r = 0; r < 16; ++r) { p0[r] = 0.f; p1[r] = 0.f; }
;                     const LAS unsigned char* Ks = K_lds + buf * SHM_K;
;                     bf16x8 kf[2][4], qx[2][2];
;     ...
;                     MLA_KREAD(0);
; #pragma unroll
;                     for (int g = 0; g < 6; ++g) {
;                         if (g + 1 < 6) MLA_KREAD(g + 1);
;                         FA_SBAR();
; #pragma unroll
;                         for (int e = 0; e < 2; ++e) { const int d0 = 2 * g + e; const bf16x8 qv = (d0 < 8) ? qr[d0 < 8 ? d0 : 0] : qx[g & 1][e];
;                             p0 = __builtin_amdgcn_mfma_f32_32x32x16_bf16(kf[g & 1][2 * e], qv, p0, 0, 0, 0);
;                             p1 = __builtin_amdgcn_mfma_f32_32x32x16_bf16(kf[g & 1][2 * e + 1], qv, p1, 0, 0, 0); }
;                         FA_SBAR(); }
.LBB0_1127:
	s_cmp_eq_u32 s32, 0
	s_cbranch_scc1 .Lmla_A
	s_cmp_eq_u32 s50, 1
	s_cbranch_scc1 .Lmla_A
	s_add_i32 s6, s50, -2
	s_add_i32 s6, s6, s45
	s_mov_b32 s99, s69
	s_branch .Lmla_B
.Lmla_A:
	s_cmp_gt_u32 s50, s44
	s_cbranch_scc1 .Lmla_C
	s_add_i32 s6, s50, -1
	s_and_b32 s51, s6, 1
	s_mul_i32 s7, s51, 0x6000
	s_add_i32 s7, s7, 0
	v_add_u32_e32 v0, s7, v200
	v_add_u32_e32 v14, s7, v201
	v_add_u32_e32 v15, s7, v202
	v_add_u32_e32 v218, s7, v203
	ds_read_b128 v[2:5], v0
	ds_read_b128 v[6:9], v0 offset:12288
	ds_read_b128 v[10:13], v14
	ds_read_b128 v[236:239], v14 offset:12288
	ds_read_b128 v[240:243], v15
	ds_read_b128 v[244:247], v15 offset:12288
	ds_read_b128 v[248:251], v218
	ds_read_b128 v[182:185], v218 offset:12288
	s_waitcnt lgkmcnt(7)
	v_mfma_f32_32x32x16_bf16 v[96:111], v[2:5], v[112:115], 0
	s_waitcnt lgkmcnt(6)
	v_mfma_f32_32x32x16_bf16 v[80:95], v[6:9], v[112:115], 0
	s_waitcnt lgkmcnt(5)
	v_mfma_f32_32x32x16_bf16 v[96:111], v[10:13], v[116:119], v[96:111]
	s_waitcnt lgkmcnt(4)
	v_mfma_f32_32x32x16_bf16 v[80:95], v[236:239], v[116:119], v[80:95]
	ds_read_b128 v[2:5], v0 offset:128
	ds_read_b128 v[6:9], v0 offset:12416
	ds_read_b128 v[10:13], v14 offset:128
	ds_read_b128 v[236:239], v14 offset:12416
	s_waitcnt lgkmcnt(7)
	v_mfma_f32_32x32x16_bf16 v[96:111], v[240:243], v[120:123], v[96:111]
	s_waitcnt lgkmcnt(6)
	v_mfma_f32_32x32x16_bf16 v[80:95], v[244:247], v[120:123], v[80:95]
	s_waitcnt lgkmcnt(5)
	v_mfma_f32_32x32x16_bf16 v[96:111], v[248:251], v[124:127], v[96:111]
	s_waitcnt lgkmcnt(4)
	v_mfma_f32_32x32x16_bf16 v[80:95], v[182:185], v[124:127], v[80:95]
	ds_read_b128 v[182:185], v15 offset:128
	ds_read_b128 v[240:243], v15 offset:12416
	ds_read_b128 v[244:247], v218 offset:128
	ds_read_b128 v[248:251], v218 offset:12416
	s_waitcnt lgkmcnt(7)
	v_mfma_f32_32x32x16_bf16 v[96:111], v[2:5], v[128:131], v[96:111]
	s_waitcnt lgkmcnt(6)
	v_mfma_f32_32x32x16_bf16 v[80:95], v[6:9], v[128:131], v[80:95]
	s_waitcnt lgkmcnt(5)
	v_mfma_f32_32x32x16_bf16 v[96:111], v[10:13], v[132:135], v[96:111]
	s_waitcnt lgkmcnt(4)
	v_mfma_f32_32x32x16_bf16 v[80:95], v[236:239], v[132:135], v[80:95]
	ds_read_b128 v[2:5], v0 offset:256
	ds_read_b128 v[6:9], v0 offset:12544
	ds_read_b128 v[10:13], v14 offset:256
	ds_read_b128 v[236:239], v14 offset:12544
	ds_read_b128 v[186:189], v214
	ds_read_b128 v[178:181], v214 offset:1024
	s_waitcnt lgkmcnt(9)
	v_mfma_f32_32x32x16_bf16 v[96:111], v[182:185], v[136:139], v[96:111]
	s_waitcnt lgkmcnt(8)
	v_mfma_f32_32x32x16_bf16 v[80:95], v[240:243], v[136:139], v[80:95]
	s_waitcnt lgkmcnt(7)
	v_mfma_f32_32x32x16_bf16 v[96:111], v[244:247], v[140:143], v[96:111]
	s_waitcnt lgkmcnt(6)
	v_mfma_f32_32x32x16_bf16 v[80:95], v[248:251], v[140:143], v[80:95]
	ds_read_b128 v[182:185], v15 offset:256
	ds_read_b128 v[240:243], v15 offset:12544
	ds_read_b128 v[244:247], v218 offset:256
	ds_read_b128 v[248:251], v218 offset:12544
	ds_read_b128 v[226:229], v214 offset:2048
	ds_read_b128 v[218:221], v214 offset:3072
	s_waitcnt lgkmcnt(7)
	v_mfma_f32_32x32x16_bf16 v[96:111], v[2:5], v[186:189], v[96:111]
	v_mfma_f32_32x32x16_bf16 v[80:95], v[6:9], v[186:189], v[80:95]
	s_waitcnt lgkmcnt(6)
	v_mfma_f32_32x32x16_bf16 v[96:111], v[10:13], v[178:181], v[96:111]
	v_mfma_f32_32x32x16_bf16 v[80:95], v[236:239], v[178:181], v[80:95]
	s_waitcnt lgkmcnt(1)
	v_mfma_f32_32x32x16_bf16 v[96:111], v[182:185], v[226:229], v[96:111]
	v_mfma_f32_32x32x16_bf16 v[80:95], v[240:243], v[226:229], v[80:95]
	s_waitcnt lgkmcnt(0)
	v_mfma_f32_32x32x16_bf16 v[96:111], v[244:247], v[218:221], v[96:111]
	v_mfma_f32_32x32x16_bf16 v[80:95], v[248:251], v[218:221], v[80:95]
	s_add_i32 s6, s6, s45
	s_mov_b32 s99, s94
	s_cmp_lg_u32 s32, 0
	s_cbranch_scc1 .Lmla_C
; __device__ __forceinline__ int crow(int r, int hi) { return (r & 3) + 8 * (r >> 2) + 4 * hi; }
; __device__ __forceinline__ void mla_attn_phase(LAS unsigned char* lds, const bf16* Q, const bf16* KV, const bf16* Z, bf16* Oabc, const float* ropec, const float* ropes, int vcu, int G, int tid) {
;     ...
;                     if (tt >= 0) { const int rrel = 32 * wid + r32 - 64 * tt;
; #pragma unroll
;                         for (int r = 0; r < 16; ++r) { const int kk = crow(r, hi); if (kk > rrel) p0[r] = -1e30f; if (32 + kk > rrel) p1[r] = -1e30f; } }
.Lmla_B:
	s_cmp_lt_i32 s6, 0
	s_cbranch_scc1 .LBB0_1129
	v_or_b32_e32 v0, 32, v211
	v_cmp_le_i32_e32 vcc, v0, v215
	v_or_b32_e32 v0, 33, v211
	s_nop 5
	v_cndmask_b32_e32 v80, v231, v80, vcc
	v_cmp_lt_i32_e32 vcc, v211, v215
	s_nop 1
	v_cndmask_b32_e32 v97, v231, v97, vcc
	v_cmp_le_i32_e32 vcc, v211, v215
	s_nop 1
	v_cndmask_b32_e32 v96, v231, v96, vcc
	v_cmp_le_i32_e32 vcc, v0, v215
	v_or_b32_e32 v0, 2, v211
	s_nop 0
	v_cndmask_b32_e32 v81, v231, v81, vcc
	v_cmp_le_i32_e32 vcc, v0, v215
	v_or_b32_e32 v0, 34, v211
	s_nop 0
	v_cndmask_b32_e32 v98, v231, v98, vcc
	v_cmp_le_i32_e32 vcc, v0, v215
	v_or_b32_e32 v0, 3, v211
	s_nop 0
	v_cndmask_b32_e32 v82, v231, v82, vcc
	v_cmp_le_i32_e32 vcc, v0, v215
	v_or_b32_e32 v0, 35, v211
	s_nop 0
	v_cndmask_b32_e32 v99, v231, v99, vcc
	v_cmp_le_i32_e32 vcc, v0, v215
	v_or_b32_e32 v0, 8, v211
	s_nop 0
	v_cndmask_b32_e32 v83, v231, v83, vcc
	v_cmp_le_i32_e32 vcc, v0, v215
	v_or_b32_e32 v0, 40, v211
	s_nop 0
	v_cndmask_b32_e32 v100, v231, v100, vcc
	v_cmp_le_i32_e32 vcc, v0, v215
	v_or_b32_e32 v0, 9, v211
	s_nop 0
	v_cndmask_b32_e32 v84, v231, v84, vcc
	v_cmp_le_i32_e32 vcc, v0, v215
	v_or_b32_e32 v0, 41, v211
	s_nop 0
	v_cndmask_b32_e32 v101, v231, v101, vcc
	v_cmp_le_i32_e32 vcc, v0, v215
	v_or_b32_e32 v0, 10, v211
	s_nop 0
	v_cndmask_b32_e32 v85, v231, v85, vcc
	v_cmp_le_i32_e32 vcc, v0, v215
	v_or_b32_e32 v0, 42, v211
	s_nop 0
	v_cndmask_b32_e32 v102, v231, v102, vcc
	v_cmp_le_i32_e32 vcc, v0, v215
	v_or_b32_e32 v0, 11, v211
	s_nop 0
	v_cndmask_b32_e32 v86, v231, v86, vcc
	v_cmp_le_i32_e32 vcc, v0, v215
	v_or_b32_e32 v0, 43, v211
	s_nop 0
	v_cndmask_b32_e32 v103, v231, v103, vcc
	v_cmp_le_i32_e32 vcc, v0, v215
	v_or_b32_e32 v0, 16, v211
	s_nop 0
	v_cndmask_b32_e32 v87, v231, v87, vcc
	v_cmp_le_i32_e32 vcc, v0, v215
	v_or_b32_e32 v0, 48, v211
	s_nop 0
	v_cndmask_b32_e32 v104, v231, v104, vcc
	v_cmp_le_i32_e32 vcc, v0, v215
	v_or_b32_e32 v0, 17, v211
	s_nop 0
	v_cndmask_b32_e32 v88, v231, v88, vcc
	v_cmp_le_i32_e32 vcc, v0, v215
	v_or_b32_e32 v0, 49, v211
	s_nop 0
	v_cndmask_b32_e32 v105, v231, v105, vcc
	v_cmp_le_i32_e32 vcc, v0, v215
	v_or_b32_e32 v0, 18, v211
	s_nop 0
	v_cndmask_b32_e32 v89, v231, v89, vcc
	v_cmp_le_i32_e32 vcc, v0, v215
	v_or_b32_e32 v0, 50, v211
	s_nop 0
	v_cndmask_b32_e32 v106, v231, v106, vcc
	v_cmp_le_i32_e32 vcc, v0, v215
	v_or_b32_e32 v0, 19, v211
	s_nop 0
	v_cndmask_b32_e32 v90, v231, v90, vcc
	v_cmp_le_i32_e32 vcc, v0, v215
	v_or_b32_e32 v0, 51, v211
	s_nop 0
	v_cndmask_b32_e32 v107, v231, v107, vcc
	v_cmp_le_i32_e32 vcc, v0, v215
	v_or_b32_e32 v0, 24, v211
	s_nop 0
	v_cndmask_b32_e32 v91, v231, v91, vcc
	v_cmp_le_i32_e32 vcc, v0, v215
	v_or_b32_e32 v0, 56, v211
	s_nop 0
	v_cndmask_b32_e32 v108, v231, v108, vcc
	v_cmp_le_i32_e32 vcc, v0, v215
	v_or_b32_e32 v0, 25, v211
	s_nop 0
	v_cndmask_b32_e32 v92, v231, v92, vcc
	v_cmp_le_i32_e32 vcc, v0, v215
	v_or_b32_e32 v0, 57, v211
	s_nop 0
	v_cndmask_b32_e32 v109, v231, v109, vcc
	v_cmp_le_i32_e32 vcc, v0, v215
	v_or_b32_e32 v0, 26, v211
	s_nop 0
	v_cndmask_b32_e32 v93, v231, v93, vcc
	v_cmp_le_i32_e32 vcc, v0, v215
	v_or_b32_e32 v0, 58, v211
	s_nop 0
	v_cndmask_b32_e32 v110, v231, v110, vcc
	v_cmp_le_i32_e32 vcc, v0, v215
	v_or_b32_e32 v0, 27, v211
	s_nop 0
	v_cndmask_b32_e32 v94, v231, v94, vcc
	v_cmp_le_i32_e32 vcc, v0, v215
	v_or_b32_e32 v0, 59, v211
	s_nop 0
	v_cndmask_b32_e32 v111, v231, v111, vcc
	v_cmp_le_i32_e32 vcc, v0, v215
	s_nop 1
	v_cndmask_b32_e32 v95, v231, v95, vcc

; #define FA_SBAR() __builtin_amdgcn_sched_barrier(0)
; __device__ __forceinline__ void finishSM(f32x16& p0, f32x16& p1, float alpha, float& l_reg, bf16x8& pa0, bf16x8& pa1, bf16x8& pa2, bf16x8& pa3) {
; #pragma unroll
;   for (int r = 0; r < 16; ++r) p1[r] = __builtin_amdgcn_exp2f(p1[r]);
;   float ps = 0;
; #pragma unroll
;   for (int r = 0; r < 16; ++r) ps += p0[r];
; #pragma unroll
;   for (int r = 0; r < 16; ++r) ps += p1[r];
;   { auto rr = __builtin_amdgcn_permlane32_swap(__float_as_uint(ps), __float_as_uint(ps), false, false);
;     ps = __uint_as_float(rr[0]) + __uint_as_float(rr[1]); }
;   l_reg = l_reg * alpha + ps;
;   FA_PK4(p0, 0, pa0); FA_PK4(p0, 8, pa1); FA_PK4(p1, 0, pa2); FA_PK4(p1, 8, pa3);
; }
; __device__ __forceinline__ int v_st(int k, int c) { const int kk = (k & ~0xC) | ((k & 4) << 1) | ((k & 8) >> 1); return ((kk >> 3) * 4 + (c >> 5)) * 512 + ((kk & 7) * 32 + (c & 31)) * 2; }
; __device__ __forceinline__ int v_rd_base(int lane) { return ((lane & 3) << 3) | (((lane >> 2) & 3) << 6) | (((lane >> 4) & 1) << 5) | (((lane >> 5) & 1) << 8); }
; template <int OFF> __device__ __forceinline__ s16x4 tr_read(int vb) {
;   s16x4 r; asm volatile("ds_read_b64_tr_b16 %0, %1 offset:%2" : "=&v"(r) : "v"(vb), "i"(OFF) : "memory"); return r;
; }
;   s16x4 l0 = tr_read<BASE + v_rd_off(D0, 0, 0)>(vb), h0 = tr_read<BASE + v_rd_off(D0, 0, 1)>(vb), l1 = tr_read<BASE + v_rd_off(D0, 1, 0)>(vb), h1 = tr_read<BASE + v_rd_off(D0, 1, 1)>(vb);
;   s16x4 l2 = tr_read<BASE + v_rd_off(D0, 2, 0)>(vb), h2 = tr_read<BASE + v_rd_off(D0, 2, 1)>(vb), l3 = tr_read<BASE + v_rd_off(D0, 3, 0)>(vb), h3 = tr_read<BASE + v_rd_off(D0, 3, 1)>(vb);
;   asm volatile("s_waitcnt lgkmcnt(0)" : "+v"(l0), "+v"(h0), "+v"(l1), "+v"(h1), "+v"(l2), "+v"(h2), "+v"(l3), "+v"(h3) :: "memory"); FA_SBAR();
;     ...
;   od = __builtin_amdgcn_mfma_f32_32x32x16_bf16(pa0, FA_PK(l0, h0), od, 0, 0, 0);
;   od = __builtin_amdgcn_mfma_f32_32x32x16_bf16(pa1, FA_PK(l1, h1), od, 0, 0, 0);
;   od = __builtin_amdgcn_mfma_f32_32x32x16_bf16(pa2, FA_PK(l2, h2), od, 0, 0, 0);
;   od = __builtin_amdgcn_mfma_f32_32x32x16_bf16(pa3, FA_PK(l3, h3), od, 0, 0, 0);
;     ...
; }
.LBB0_1133:
	v_cndmask_b32_e64 v216, v2, v216, s[6:7]
	v_mul_f32_e32 v2, 0xbdd53b94, v216
	v_fmamk_f32 v3, v96, 0x3dd53b94, v2
	v_fmamk_f32 v4, v97, 0x3dd53b94, v2
	v_exp_f32_e32 v3, v3
	v_fmamk_f32 v5, v98, 0x3dd53b94, v2
	v_exp_f32_e32 v4, v4
	v_fmamk_f32 v6, v99, 0x3dd53b94, v2
	v_exp_f32_e32 v5, v5
	v_fmamk_f32 v7, v100, 0x3dd53b94, v2
	v_fmamk_f32 v8, v101, 0x3dd53b94, v2
	v_fmamk_f32 v9, v102, 0x3dd53b94, v2
	v_fmamk_f32 v10, v103, 0x3dd53b94, v2
	v_fmamk_f32 v11, v104, 0x3dd53b94, v2
	v_fmamk_f32 v12, v105, 0x3dd53b94, v2
	v_fmamk_f32 v13, v106, 0x3dd53b94, v2
	v_fmamk_f32 v14, v107, 0x3dd53b94, v2
	v_fmamk_f32 v15, v108, 0x3dd53b94, v2
	v_fmamk_f32 v96, v109, 0x3dd53b94, v2
	v_fmamk_f32 v97, v110, 0x3dd53b94, v2
	v_fmamk_f32 v98, v111, 0x3dd53b94, v2
	v_fmamk_f32 v80, v80, 0x3dd53b94, v2
	v_fmamk_f32 v81, v81, 0x3dd53b94, v2
	v_fmamk_f32 v82, v82, 0x3dd53b94, v2
	v_fmamk_f32 v83, v83, 0x3dd53b94, v2
	v_fmamk_f32 v84, v84, 0x3dd53b94, v2
	v_fmamk_f32 v85, v85, 0x3dd53b94, v2
	v_fmamk_f32 v86, v86, 0x3dd53b94, v2
	v_fmamk_f32 v87, v87, 0x3dd53b94, v2
	v_fmamk_f32 v88, v88, 0x3dd53b94, v2
	v_fmamk_f32 v89, v89, 0x3dd53b94, v2
	v_fmamk_f32 v90, v90, 0x3dd53b94, v2
	v_fmamk_f32 v91, v91, 0x3dd53b94, v2
	v_fmamk_f32 v92, v92, 0x3dd53b94, v2
	v_fmamk_f32 v93, v93, 0x3dd53b94, v2
	v_fmamk_f32 v94, v94, 0x3dd53b94, v2
	v_fmac_f32_e32 v2, 0x3dd53b94, v95
	v_exp_f32_e32 v95, v6
	v_exp_f32_e32 v99, v7
	v_exp_f32_e32 v100, v2
	v_add_f32_e32 v2, 0, v3
	v_exp_f32_e32 v8, v8
	v_add_f32_e32 v2, v4, v2
	v_exp_f32_e32 v9, v9
	v_add_f32_e32 v2, v5, v2
	v_exp_f32_e32 v10, v10
	v_add_f32_e32 v2, v95, v2
	v_exp_f32_e32 v11, v11
	v_add_f32_e32 v2, v99, v2
	v_exp_f32_e32 v12, v12
	v_add_f32_e32 v2, v8, v2
	v_exp_f32_e32 v13, v13
	v_add_f32_e32 v2, v9, v2
	v_exp_f32_e32 v14, v14
	v_add_f32_e32 v2, v10, v2
	v_exp_f32_e32 v15, v15
	v_add_f32_e32 v2, v11, v2
	v_exp_f32_e32 v96, v96
	v_add_f32_e32 v2, v12, v2
	v_exp_f32_e32 v97, v97
	v_add_f32_e32 v2, v13, v2
	v_exp_f32_e32 v98, v98
	v_add_f32_e32 v2, v14, v2
	v_exp_f32_e32 v80, v80
	v_add_f32_e32 v2, v15, v2
	v_exp_f32_e32 v81, v81
	v_add_f32_e32 v2, v96, v2
	v_exp_f32_e32 v82, v82
	v_add_f32_e32 v2, v97, v2
	v_exp_f32_e32 v83, v83
	v_add_f32_e32 v2, v98, v2
	v_exp_f32_e32 v84, v84
	v_add_f32_e32 v2, v80, v2
	v_exp_f32_e32 v85, v85
	v_add_f32_e32 v2, v81, v2
	v_exp_f32_e32 v86, v86
	v_add_f32_e32 v2, v82, v2
	v_exp_f32_e32 v87, v87
	v_add_f32_e32 v2, v83, v2
	v_exp_f32_e32 v88, v88
	v_add_f32_e32 v2, v84, v2
	v_exp_f32_e32 v89, v89
	v_add_f32_e32 v2, v85, v2
	v_exp_f32_e32 v90, v90
	v_add_f32_e32 v2, v86, v2
	v_exp_f32_e32 v91, v91
	v_add_f32_e32 v2, v87, v2
	v_exp_f32_e32 v92, v92
	v_add_f32_e32 v2, v88, v2
	v_exp_f32_e32 v93, v93
	v_add_f32_e32 v2, v89, v2
	v_exp_f32_e32 v94, v94
	v_add_f32_e32 v2, v90, v2
	v_add_f32_e32 v2, v91, v2
	v_add_f32_e32 v2, v92, v2
	v_add_f32_e32 v2, v93, v2
	v_add_f32_e32 v2, v94, v2
	v_add_f32_e32 v6, v100, v2
	v_mov_b32_e32 v7, v6
	s_nop 1
	v_permlane32_swap_b32_e32 v6, v7
	v_cvt_pk_bf16_f32 v2, v3, v4
	v_cvt_pk_bf16_f32 v3, v5, v95
	v_cvt_pk_bf16_f32 v4, v99, v8
	v_cvt_pk_bf16_f32 v5, v9, v10
	v_cvt_pk_bf16_f32 v8, v11, v12
	v_cvt_pk_bf16_f32 v9, v13, v14
	v_cvt_pk_bf16_f32 v10, v15, v96
	v_cvt_pk_bf16_f32 v11, v97, v98
	v_cvt_pk_bf16_f32 v12, v80, v81
	v_cvt_pk_bf16_f32 v13, v82, v83
	v_cvt_pk_bf16_f32 v14, v84, v85
	v_cvt_pk_bf16_f32 v15, v86, v87
	v_cvt_pk_bf16_f32 v80, v88, v89
	v_cvt_pk_bf16_f32 v81, v90, v91
	v_cvt_pk_bf16_f32 v82, v92, v93
	v_cvt_pk_bf16_f32 v83, v94, v100
	s_nop 0
	v_permlane32_swap_b32_e32 v2, v4
	v_permlane32_swap_b32_e32 v3, v5
	v_permlane32_swap_b32_e32 v8, v10
	v_permlane32_swap_b32_e32 v9, v11
	v_permlane32_swap_b32_e32 v12, v14
	v_permlane32_swap_b32_e32 v13, v15
	v_permlane32_swap_b32_e32 v80, v82
	v_permlane32_swap_b32_e32 v81, v83
	v_add_u32_e32 v100, s99, v213
	ds_read_b64_tr_b16 v[84:85], v100 offset:0
	ds_read_b64_tr_b16 v[86:87], v100 offset:0x800
	ds_read_b64_tr_b16 v[88:89], v100 offset:0x1000
	ds_read_b64_tr_b16 v[90:91], v100 offset:0x1800
	ds_read_b64_tr_b16 v[92:93], v100 offset:0x2000
	ds_read_b64_tr_b16 v[94:95], v100 offset:0x2800
	ds_read_b64_tr_b16 v[96:97], v100 offset:0x3000
	ds_read_b64_tr_b16 v[98:99], v100 offset:0x3800
	s_nop 0
	s_waitcnt lgkmcnt(6)
	s_nop 0
	v_mfma_f32_32x32x16_bf16 v[64:79], v[2:5], v[84:87], v[64:79]
	ds_read_b64_tr_b16 v[84:85], v100 offset:0x200
	ds_read_b64_tr_b16 v[86:87], v100 offset:0xa00
	s_waitcnt lgkmcnt(6)
	v_mfma_f32_32x32x16_bf16 v[64:79], v[8:11], v[88:91], v[64:79]
	ds_read_b64_tr_b16 v[88:89], v100 offset:0x1200
	ds_read_b64_tr_b16 v[90:91], v100 offset:0x1a00
	s_waitcnt lgkmcnt(6)
	v_mfma_f32_32x32x16_bf16 v[64:79], v[12:15], v[92:95], v[64:79]
	ds_read_b64_tr_b16 v[92:93], v100 offset:0x2200
	ds_read_b64_tr_b16 v[94:95], v100 offset:0x2a00
	s_waitcnt lgkmcnt(6)
	v_mfma_f32_32x32x16_bf16 v[64:79], v[80:83], v[96:99], v[64:79]
	ds_read_b64_tr_b16 v[96:97], v100 offset:0x3200
	ds_read_b64_tr_b16 v[98:99], v100 offset:0x3a00
	s_nop 0
	s_waitcnt lgkmcnt(6)
	s_nop 0
	v_mfma_f32_32x32x16_bf16 v[48:63], v[2:5], v[84:87], v[48:63]
	ds_read_b64_tr_b16 v[84:85], v100 offset:0x400
	ds_read_b64_tr_b16 v[86:87], v100 offset:0xc00
	s_waitcnt lgkmcnt(6)
	v_mfma_f32_32x32x16_bf16 v[48:63], v[8:11], v[88:91], v[48:63]
	ds_read_b64_tr_b16 v[88:89], v100 offset:0x1400
	ds_read_b64_tr_b16 v[90:91], v100 offset:0x1c00
	s_waitcnt lgkmcnt(6)
	v_mfma_f32_32x32x16_bf16 v[48:63], v[12:15], v[92:95], v[48:63]
	ds_read_b64_tr_b16 v[92:93], v100 offset:0x2400
	ds_read_b64_tr_b16 v[94:95], v100 offset:0x2c00
	s_waitcnt lgkmcnt(6)
	v_mfma_f32_32x32x16_bf16 v[48:63], v[80:83], v[96:99], v[48:63]
	ds_read_b64_tr_b16 v[96:97], v100 offset:0x3400
	ds_read_b64_tr_b16 v[98:99], v100 offset:0x3c00
	s_nop 0
	s_waitcnt lgkmcnt(6)
	s_nop 0
	v_mfma_f32_32x32x16_bf16 v[32:47], v[2:5], v[84:87], v[32:47]
	ds_read_b64_tr_b16 v[84:85], v100 offset:0x600
	ds_read_b64_tr_b16 v[86:87], v100 offset:0xe00
	s_waitcnt lgkmcnt(6)
	v_mfma_f32_32x32x16_bf16 v[32:47], v[8:11], v[88:91], v[32:47]
	ds_read_b64_tr_b16 v[88:89], v100 offset:0x1600
	ds_read_b64_tr_b16 v[90:91], v100 offset:0x1e00
	s_waitcnt lgkmcnt(6)
	v_mfma_f32_32x32x16_bf16 v[32:47], v[12:15], v[92:95], v[32:47]
	ds_read_b64_tr_b16 v[92:93], v100 offset:0x2600
	ds_read_b64_tr_b16 v[94:95], v100 offset:0x2e00
	s_waitcnt lgkmcnt(6)
	v_mfma_f32_32x32x16_bf16 v[32:47], v[80:83], v[96:99], v[32:47]
	ds_read_b64_tr_b16 v[96:97], v100 offset:0x3600
	ds_read_b64_tr_b16 v[98:99], v100 offset:0x3e00
	s_nop 0
	s_waitcnt lgkmcnt(6)
	s_nop 0
	v_mfma_f32_32x32x16_bf16 v[16:31], v[2:5], v[84:87], v[16:31]
	s_andn2_b64 vcc, exec, s[14:15]
	s_waitcnt lgkmcnt(4)
	v_mfma_f32_32x32x16_bf16 v[16:31], v[8:11], v[88:91], v[16:31]
	s_waitcnt lgkmcnt(2)
	v_mfma_f32_32x32x16_bf16 v[16:31], v[12:15], v[92:95], v[16:31]
	s_waitcnt lgkmcnt(0)
	v_mfma_f32_32x32x16_bf16 v[16:31], v[80:83], v[96:99], v[16:31]
	v_add_f32_e32 v2, v6, v7
	v_fmac_f32_e32 v2, v217, v0
	v_mov_b32_e32 v217, v2
	s_cmp_lg_u32 s32, 0
	s_cbranch_scc1 .Lmla_A
; #define MLA_SWRITE(bb) do { *(LAS v4u*)(V_lds + (bb) * SHM_V + vst0) = vs0; *(LAS v4u*)(V_lds + (bb) * SHM_V + vst0 + 8192) = vs1; \
;             *(LAS v4u*)(K_lds + (bb) * SHM_K + kst0) = ks0; *(LAS v4u*)(K_lds + (bb) * SHM_K + kst0 + 32 * 384) = ks1; \
;             *(LAS v4u*)(K_lds + (bb) * SHM_K + kst2) = krr; } while (0)
; __device__ __forceinline__ void mla_attn_phase(LAS unsigned char* lds, const bf16* Q, const bf16* KV, const bf16* Z, bf16* Oabc, const float* ropec, const float* ropes, int vcu, int G, int tid) {
;     ...
;                 if (t + 1 < nt) MLA_SWRITE(buf ^ 1);
;                 __syncthreads();
;             }
;     ...
;             if (hi == 0) li_l[r32] = l_reg;
.Lmla_C:
	s_andn2_b64 vcc, exec, s[14:15]
	s_cbranch_vccnz .LBB0_1135
	s_xor_b32 s6, s51, 1
	v_add_u32_e32 v2, s98, v210
	s_mulk_i32 s6, 0x6000
	s_add_i32 s6, s6, 0
	s_waitcnt vmcnt(3)
	ds_write_b128 v2, v[148:151] offset:49152
	s_waitcnt vmcnt(1)
	ds_write_b128 v2, v[156:159] offset:57344
	v_add_u32_e32 v2, s6, v204
	ds_write_b128 v2, v[144:147]
	ds_write_b128 v2, v[152:155] offset:12288
	v_add_u32_e32 v2, s6, v199
	s_waitcnt vmcnt(0)
	ds_write_b128 v2, v[160:163]
.LBB0_1135:
	s_mov_b32 s99, s69
	s_mov_b32 s69, s94
	s_mov_b32 s94, s98
	s_mov_b32 s98, s99
	s_add_i32 s50, s50, 1
	s_mov_b64 s[6:7], 0x88000
	v_lshl_add_u64 v[196:197], v[196:197], 0, s[6:7]
	s_add_i32 s6, s45, s50
	v_subrev_u32_e32 v215, 64, v215
	s_cmp_eq_u32 s6, 6
	v_lshl_add_u64 v[194:195], v[194:195], 0, s[62:63]
	s_waitcnt lgkmcnt(0)
	s_barrier
	s_cbranch_scc0 .LBB0_1125
	s_and_saveexec_b64 s[6:7], s[4:5]
	s_cbranch_execz .LBB0_1123
	ds_write_b32 v212, v217
	s_branch .LBB0_1123

; #define LAS __attribute__((address_space(3)))
; __global__ void __launch_bounds__(NWAVES * 64, 2) fwd_kernel(Args args) {
;     extern __shared__ __attribute__((aligned(16))) unsigned char lds_raw[];
;     LAS unsigned char* lds = (LAS unsigned char*)lds_raw;
	.amdhsa_kernel _Z10fwd_kernel4Args
		.amdhsa_group_segment_fixed_size 16384
		.amdhsa_private_segment_fixed_size 0
		.amdhsa_kernarg_size 496
		.amdhsa_user_sgpr_count 2
		.amdhsa_user_sgpr_dispatch_ptr 0
		.amdhsa_user_sgpr_queue_ptr 0
		.amdhsa_user_sgpr_kernarg_segment_ptr 1
		.amdhsa_user_sgpr_dispatch_id 0
		.amdhsa_user_sgpr_kernarg_preload_length 0
		.amdhsa_user_sgpr_kernarg_preload_offset 0
		.amdhsa_user_sgpr_private_segment_size 0
		.amdhsa_uses_dynamic_stack 0
		.amdhsa_enable_private_segment 0
		.amdhsa_system_sgpr_workgroup_id_x 1
		.amdhsa_system_sgpr_workgroup_id_y 0
		.amdhsa_system_sgpr_workgroup_id_z 0
		.amdhsa_system_sgpr_workgroup_info 0
		.amdhsa_system_vgpr_workitem_id 0
		.amdhsa_next_free_vgpr 256
		.amdhsa_next_free_sgpr 100
		.amdhsa_accum_offset 256
		.amdhsa_reserve_vcc 1
		.amdhsa_float_round_mode_32 0
		.amdhsa_float_round_mode_16_64 0
		.amdhsa_float_denorm_mode_32 3
		.amdhsa_float_denorm_mode_16_64 3
		.amdhsa_dx10_clamp 1
		.amdhsa_ieee_mode 1
		.amdhsa_fp16_overflow 0
		.amdhsa_tg_split 0
		.amdhsa_exception_fp_ieee_invalid_op 0
		.amdhsa_exception_fp_denorm_src 0
		.amdhsa_exception_fp_ieee_div_zero 0
		.amdhsa_exception_fp_ieee_overflow 0
		.amdhsa_exception_fp_ieee_underflow 0
		.amdhsa_exception_fp_ieee_inexact 0
		.amdhsa_exception_int_div_zero 0
	.end_amdhsa_kernel

; #define LAS __attribute__((address_space(3)))
; __global__ void __launch_bounds__(NWAVES * 64, 2) fwd_kernel(Args args) {
;     extern __shared__ __attribute__((aligned(16))) unsigned char lds_raw[];
;     LAS unsigned char* lds = (LAS unsigned char*)lds_raw;
amdhsa.kernels:
  - .agpr_count:     0
    .args:
      - .offset:         0
        .size:           240
        .value_kind:     by_value
      - .offset:         240
        .size:           4
        .value_kind:     hidden_block_count_x
      - .offset:         244
        .size:           4
        .value_kind:     hidden_block_count_y
      - .offset:         248
        .size:           4
        .value_kind:     hidden_block_count_z
      - .offset:         252
        .size:           2
        .value_kind:     hidden_group_size_x
      - .offset:         254
        .size:           2
        .value_kind:     hidden_group_size_y
      - .offset:         256
        .size:           2
        .value_kind:     hidden_group_size_z
      - .offset:         258
        .size:           2
        .value_kind:     hidden_remainder_x
      - .offset:         260
        .size:           2
        .value_kind:     hidden_remainder_y
      - .offset:         262
        .size:           2
        .value_kind:     hidden_remainder_z
      - .offset:         280
        .size:           8
        .value_kind:     hidden_global_offset_x
      - .offset:         288
        .size:           8
        .value_kind:     hidden_global_offset_y
      - .offset:         296
        .size:           8
        .value_kind:     hidden_global_offset_z
      - .offset:         304
        .size:           2
        .value_kind:     hidden_grid_dims
      - .offset:         360
        .size:           4
        .value_kind:     hidden_dynamic_lds_size
    .group_segment_fixed_size: 16384
    .kernarg_segment_align: 8
    .kernarg_segment_size: 496
    .language:       OpenCL C
    .language_version:
      - 2
      - 0
    .max_flat_workgroup_size: 512
    .name:           _Z10fwd_kernel4Args
    .private_segment_fixed_size: 0
    .sgpr_count:     106
    .sgpr_spill_count: 268
    .symbol:         _Z10fwd_kernel4Args.kd
    .uniform_work_group_size: 1
    .uses_dynamic_stack: false
    .vgpr_count:     256
    .vgpr_spill_count: 0
    .wavefront_size: 64
